# code placement: the QKV and residual GEMM K-loop heads aligned to 64 bytes (.p2align 6; the gate|up head already was)
# baseline (speedup 1.0000x reference)
; #define PG8_STAGE(bufoff, gbase, voff) do { _Pragma("unroll") for (int _i = 0; _i < 2; ++_i) \
;         __builtin_amdgcn_global_load_lds((const unsigned*)((const char*)(gbase) + (voff)[_i]), (PG8_LAS unsigned*)(lds + (bufoff) + ldsw + _i * 8192), 16, 0, 0); } while (0)
; #define PG8_LDA(dst, b, h) do { _Pragma("unroll") for (int m = 0; m < 4; ++m) _Pragma("unroll") for (int k = 0; k < 2; ++k) dst[m][k] = *(const PG8_LAS bf16x8*)(lds + PG8_SA(b, h) + aoff + m * 2048 + k * 1024); } while (0)
; #define PG8_LDB(dst, b, h) do { _Pragma("unroll") for (int n = 0; n < 2; ++n) _Pragma("unroll") for (int k = 0; k < 2; ++k) dst[n][k] = *(const PG8_LAS bf16x8*)(lds + PG8_SB(b, h) + boff + n * 2048 + k * 1024); } while (0)
; #define PG8_MMA(ai, bj, At, Bt) do { __builtin_amdgcn_s_setprio(1); _Pragma("unroll") for (int m = 0; m < 4; ++m) _Pragma("unroll") for (int n = 0; n < 2; ++n) _Pragma("unroll") for (int k = 0; k < 2; ++k) \
;         acc[ai][bj][m][n] = __builtin_amdgcn_mfma_f32_16x16x32_bf16(Bt[n][k], At[m][k], acc[ai][bj][m][n], 0, 0, 0); __builtin_amdgcn_s_setprio(0); } while (0)
; #define PG8_WAIT_V(n) asm volatile("s_waitcnt vmcnt(" #n ")" ::: "memory")
; #define PG8_WAIT_L(n) asm volatile("s_waitcnt lgkmcnt(" #n ")" ::: "memory")
; #define PG8_BAR __builtin_amdgcn_s_barrier()
; #define PG8_SCHED __builtin_amdgcn_sched_barrier(0)
; template <class Epi, class Sched, bool ALIGN_EPI>
; __device__ __forceinline__ void gemm_phase(PG8_LAS unsigned char* lds, const Gemm g, const Sched& S, const Epi& E, const int tid) {
;     ...
;             PG8_LDB(B0, 0, 0); PG8_LDB(B1, 0, 1); PG8_SCHED; PG8_LDA(At, 0, 0); PG8_STAGE(PG8_SA(1, 1), a1 + hstepA, voffA);
;             PG8_WAIT_V(8); PG8_WAIT_L(0); PG8_BAR; PG8_MMA(0, 0, At, B0); PG8_MMA(0, 1, At, B1); PG8_BAR; PG8_SCHED;
;             PG8_LDA(At, 0, 1); PG8_STAGE(PG8_SB(0, 0), b2, voffB); PG8_STAGE(PG8_SB(0, 1), b2 + hstepB, voffB); PG8_STAGE(PG8_SA(0, 0), a2, voffA);
;             PG8_WAIT_V(8); PG8_WAIT_L(0); PG8_BAR; PG8_MMA(1, 0, At, B0); PG8_MMA(1, 1, At, B1); PG8_BAR; PG8_SCHED;
;             PG8_LDB(B0, 1, 0); PG8_LDB(B1, 1, 1); PG8_SCHED; PG8_LDA(At, 1, 0); PG8_STAGE(PG8_SA(0, 1), a2 + hstepA, voffA);
;             PG8_WAIT_V(8); PG8_WAIT_L(0); PG8_BAR; PG8_MMA(0, 0, At, B0); PG8_MMA(0, 1, At, B1); PG8_BAR; PG8_SCHED;
.Lsprio_0:
	s_barrier
	v_mfma_f32_16x16x32_bf16 v[142:145], v[80:83], v[194:197], 0
	v_mfma_f32_16x16x32_bf16 v[134:137], v[96:99], v[194:197], 0
	v_mfma_f32_16x16x32_bf16 v[124:127], v[80:83], v[202:205], 0
	v_mfma_f32_16x16x32_bf16 v[116:119], v[96:99], v[202:205], 0
	v_mfma_f32_16x16x32_bf16 v[108:111], v[80:83], v[210:213], 0
	v_mfma_f32_16x16x32_bf16 v[92:95], v[96:99], v[210:213], 0
	v_mfma_f32_16x16x32_bf16 v[76:79], v[80:83], v[218:221], 0
	v_mfma_f32_16x16x32_bf16 v[68:71], v[96:99], v[218:221], 0
	v_mfma_f32_16x16x32_bf16 v[142:145], v[84:87], v[198:201], v[142:145]
	v_mfma_f32_16x16x32_bf16 v[134:137], v[100:103], v[198:201], v[134:137]
	v_mfma_f32_16x16x32_bf16 v[124:127], v[84:87], v[206:209], v[124:127]
	v_mfma_f32_16x16x32_bf16 v[116:119], v[100:103], v[206:209], v[116:119]
	v_mfma_f32_16x16x32_bf16 v[108:111], v[84:87], v[214:217], v[108:111]
	v_mfma_f32_16x16x32_bf16 v[92:95], v[100:103], v[214:217], v[92:95]
	v_mfma_f32_16x16x32_bf16 v[76:79], v[84:87], v[222:225], v[76:79]
	v_mfma_f32_16x16x32_bf16 v[68:71], v[100:103], v[222:225], v[68:71]
	v_mfma_f32_16x16x32_bf16 v[138:141], v[162:165], v[194:197], 0
	v_mfma_f32_16x16x32_bf16 v[130:133], v[186:189], v[194:197], 0
	v_mfma_f32_16x16x32_bf16 v[120:123], v[162:165], v[202:205], 0
	v_mfma_f32_16x16x32_bf16 v[112:115], v[186:189], v[202:205], 0
	v_mfma_f32_16x16x32_bf16 v[104:107], v[162:165], v[210:213], 0
	v_mfma_f32_16x16x32_bf16 v[88:91], v[186:189], v[210:213], 0
	v_mfma_f32_16x16x32_bf16 v[72:75], v[162:165], v[218:221], 0
	v_mfma_f32_16x16x32_bf16 v[64:67], v[186:189], v[218:221], 0
	v_mfma_f32_16x16x32_bf16 v[138:141], v[182:185], v[198:201], v[138:141]
	v_mfma_f32_16x16x32_bf16 v[130:133], v[190:193], v[198:201], v[130:133]
	v_mfma_f32_16x16x32_bf16 v[120:123], v[182:185], v[206:209], v[120:123]
	v_mfma_f32_16x16x32_bf16 v[112:115], v[190:193], v[206:209], v[112:115]
	v_mfma_f32_16x16x32_bf16 v[104:107], v[182:185], v[214:217], v[104:107]
	v_mfma_f32_16x16x32_bf16 v[88:91], v[190:193], v[214:217], v[88:91]
	v_mfma_f32_16x16x32_bf16 v[72:75], v[182:185], v[222:225], v[72:75]
	v_mfma_f32_16x16x32_bf16 v[64:67], v[190:193], v[222:225], v[64:67]
	s_barrier
	s_add_i32 s63, s63, s42
	s_mov_b32 m0, s63
	ds_read_b128 v[194:197], v180 offset:16384
	ds_read_b128 v[198:201], v180 offset:17408
	ds_read_b128 v[202:205], v180 offset:18432
	ds_read_b128 v[206:209], v180 offset:19456
	ds_read_b128 v[210:213], v180 offset:20480
	ds_read_b128 v[214:217], v180 offset:21504
	ds_read_b128 v[218:221], v180 offset:22528
	ds_read_b128 v[222:225], v180 offset:23552
	global_load_lds_dwordx4 v150, s[20:21]
	s_add_i32 m0, s63, 0x2000
	s_add_u32 s64, s20, 0x4000
	s_addc_u32 s65, s21, 0
	s_add_i32 s63, s66, s42
	global_load_lds_dwordx4 v146, s[20:21]
	s_mov_b32 m0, s63
	s_nop 0
	global_load_lds_dwordx4 v150, s[64:65]
	s_add_i32 m0, s63, 0x2000
	s_nop 0
	global_load_lds_dwordx4 v146, s[64:65]
	s_mov_b32 m0, s45
	s_nop 0
	global_load_lds_dwordx4 v152, s[22:23]
	s_mov_b32 m0, s46
	s_nop 0
	global_load_lds_dwordx4 v148, s[22:23]
	s_waitcnt vmcnt(8)
	s_waitcnt lgkmcnt(0)
	s_barrier
	v_mfma_f32_16x16x32_bf16 v[60:63], v[80:83], v[194:197], 0
	v_mfma_f32_16x16x32_bf16 v[52:55], v[96:99], v[194:197], 0
	v_mfma_f32_16x16x32_bf16 v[44:47], v[80:83], v[202:205], 0
	v_mfma_f32_16x16x32_bf16 v[36:39], v[96:99], v[202:205], 0
	v_mfma_f32_16x16x32_bf16 v[28:31], v[80:83], v[210:213], 0
	v_mfma_f32_16x16x32_bf16 v[20:23], v[96:99], v[210:213], 0
	v_mfma_f32_16x16x32_bf16 v[12:15], v[80:83], v[218:221], 0
	v_mfma_f32_16x16x32_bf16 v[4:7], v[96:99], v[218:221], 0
	v_mfma_f32_16x16x32_bf16 v[60:63], v[84:87], v[198:201], v[60:63]
	v_mfma_f32_16x16x32_bf16 v[52:55], v[100:103], v[198:201], v[52:55]
	v_mfma_f32_16x16x32_bf16 v[44:47], v[84:87], v[206:209], v[44:47]
	v_mfma_f32_16x16x32_bf16 v[36:39], v[100:103], v[206:209], v[36:39]
	v_mfma_f32_16x16x32_bf16 v[28:31], v[84:87], v[214:217], v[28:31]
	v_mfma_f32_16x16x32_bf16 v[20:23], v[100:103], v[214:217], v[20:23]
	v_mfma_f32_16x16x32_bf16 v[12:15], v[84:87], v[222:225], v[12:15]
	v_mfma_f32_16x16x32_bf16 v[4:7], v[100:103], v[222:225], v[4:7]
	v_mfma_f32_16x16x32_bf16 v[56:59], v[162:165], v[194:197], 0
	v_mfma_f32_16x16x32_bf16 v[48:51], v[186:189], v[194:197], 0
	v_mfma_f32_16x16x32_bf16 v[40:43], v[162:165], v[202:205], 0
	v_mfma_f32_16x16x32_bf16 v[32:35], v[186:189], v[202:205], 0
	v_mfma_f32_16x16x32_bf16 v[24:27], v[162:165], v[210:213], 0
	v_mfma_f32_16x16x32_bf16 v[16:19], v[186:189], v[210:213], 0
	v_mfma_f32_16x16x32_bf16 v[8:11], v[162:165], v[218:221], 0
	v_mfma_f32_16x16x32_bf16 v[0:3], v[186:189], v[218:221], 0
	v_mfma_f32_16x16x32_bf16 v[56:59], v[182:185], v[198:201], v[56:59]
	v_mfma_f32_16x16x32_bf16 v[48:51], v[190:193], v[198:201], v[48:51]
	v_mfma_f32_16x16x32_bf16 v[40:43], v[182:185], v[206:209], v[40:43]
	v_mfma_f32_16x16x32_bf16 v[32:35], v[190:193], v[206:209], v[32:35]
	v_mfma_f32_16x16x32_bf16 v[24:27], v[182:185], v[214:217], v[24:27]
	v_mfma_f32_16x16x32_bf16 v[16:19], v[190:193], v[214:217], v[16:19]
	v_mfma_f32_16x16x32_bf16 v[8:11], v[182:185], v[222:225], v[8:11]
	v_mfma_f32_16x16x32_bf16 v[0:3], v[190:193], v[222:225], v[0:3]
	s_barrier
	s_add_i32 s63, 0, 0x18000
	s_add_i32 s64, 0, 0x1c000
	ds_read_b128 v[80:83], v166 offset:32768
	ds_read_b128 v[84:87], v166 offset:33792
	ds_read_b128 v[96:99], v166 offset:34816
	ds_read_b128 v[100:103], v166 offset:35840
	ds_read_b128 v[162:165], v166 offset:49152
	ds_read_b128 v[182:185], v166 offset:50176
	ds_read_b128 v[186:189], v166 offset:51200
	ds_read_b128 v[190:193], v166 offset:52224
	s_add_u32 s22, s22, 0x4000
	s_addc_u32 s23, s23, 0
	s_mov_b32 m0, s47
	ds_read_b128 v[194:197], v180 offset:32768
	ds_read_b128 v[198:201], v180 offset:33792
	ds_read_b128 v[202:205], v180 offset:34816
	ds_read_b128 v[206:209], v180 offset:35840
	ds_read_b128 v[210:213], v180 offset:36864
	ds_read_b128 v[214:217], v180 offset:37888
	ds_read_b128 v[218:221], v180 offset:38912
	ds_read_b128 v[222:225], v180 offset:39936
	global_load_lds_dwordx4 v152, s[22:23]
	s_mov_b32 m0, s48
	s_nop 0
	global_load_lds_dwordx4 v148, s[22:23]
	s_waitcnt vmcnt(8)
	s_waitcnt lgkmcnt(0)
	s_barrier
; #define PG8_STAGE(bufoff, gbase, voff) do { _Pragma("unroll") for (int _i = 0; _i < 2; ++_i) \
;         __builtin_amdgcn_global_load_lds((const unsigned*)((const char*)(gbase) + (voff)[_i]), (PG8_LAS unsigned*)(lds + (bufoff) + ldsw + _i * 8192), 16, 0, 0); } while (0)
; #define PG8_LDA(dst, b, h) do { _Pragma("unroll") for (int m = 0; m < 4; ++m) _Pragma("unroll") for (int k = 0; k < 2; ++k) dst[m][k] = *(const PG8_LAS bf16x8*)(lds + PG8_SA(b, h) + aoff + m * 2048 + k * 1024); } while (0)
; #define PG8_LDB(dst, b, h) do { _Pragma("unroll") for (int n = 0; n < 2; ++n) _Pragma("unroll") for (int k = 0; k < 2; ++k) dst[n][k] = *(const PG8_LAS bf16x8*)(lds + PG8_SB(b, h) + boff + n * 2048 + k * 1024); } while (0)
; #define PG8_MMA(ai, bj, At, Bt) do { __builtin_amdgcn_s_setprio(1); _Pragma("unroll") for (int m = 0; m < 4; ++m) _Pragma("unroll") for (int n = 0; n < 2; ++n) _Pragma("unroll") for (int k = 0; k < 2; ++k) \
;         acc[ai][bj][m][n] = __builtin_amdgcn_mfma_f32_16x16x32_bf16(Bt[n][k], At[m][k], acc[ai][bj][m][n], 0, 0, 0); __builtin_amdgcn_s_setprio(0); } while (0)
; #define PG8_WAIT_V(n) asm volatile("s_waitcnt vmcnt(" #n ")" ::: "memory")
; #define PG8_WAIT_L(n) asm volatile("s_waitcnt lgkmcnt(" #n ")" ::: "memory")
; #define PG8_BAR __builtin_amdgcn_s_barrier()
; #define PG8_SCHED __builtin_amdgcn_sched_barrier(0)
; template <class Epi, class Sched, bool ALIGN_EPI>
; __device__ __forceinline__ void gemm_phase(PG8_LAS unsigned char* lds, const Gemm g, const Sched& S, const Epi& E, const int tid) {
;     ...
;             PG8_LDB(B0, 1, 0); PG8_LDB(B1, 1, 1); PG8_SCHED; PG8_LDA(At, 1, 0); PG8_STAGE(PG8_SA(0, 1), a2 + hstepA, voffA);
;             PG8_WAIT_V(8); PG8_WAIT_L(0); PG8_BAR; PG8_MMA(0, 0, At, B0); PG8_MMA(0, 1, At, B1); PG8_BAR; PG8_SCHED;
;             PG8_LDA(At, 1, 1); PG8_STAGE(PG8_SB(1, 0), b3, voffB); PG8_STAGE(PG8_SB(1, 1), b3 + hstepB, voffB); PG8_STAGE(PG8_SA(1, 0), a3, voffA);
;             PG8_WAIT_V(8); PG8_WAIT_L(0); PG8_BAR; PG8_MMA(1, 0, At, B0); PG8_MMA(1, 1, At, B1); PG8_BAR; PG8_SCHED;
;         }
	v_mfma_f32_16x16x32_bf16 v[142:145], v[80:83], v[194:197], v[142:145]
	v_mfma_f32_16x16x32_bf16 v[134:137], v[96:99], v[194:197], v[134:137]
	v_mfma_f32_16x16x32_bf16 v[124:127], v[80:83], v[202:205], v[124:127]
	v_mfma_f32_16x16x32_bf16 v[116:119], v[96:99], v[202:205], v[116:119]
	v_mfma_f32_16x16x32_bf16 v[108:111], v[80:83], v[210:213], v[108:111]
	v_mfma_f32_16x16x32_bf16 v[92:95], v[96:99], v[210:213], v[92:95]
	v_mfma_f32_16x16x32_bf16 v[76:79], v[80:83], v[218:221], v[76:79]
	v_mfma_f32_16x16x32_bf16 v[68:71], v[96:99], v[218:221], v[68:71]
	v_mfma_f32_16x16x32_bf16 v[142:145], v[84:87], v[198:201], v[142:145]
	v_mfma_f32_16x16x32_bf16 v[134:137], v[100:103], v[198:201], v[134:137]
	v_mfma_f32_16x16x32_bf16 v[124:127], v[84:87], v[206:209], v[124:127]
	v_mfma_f32_16x16x32_bf16 v[116:119], v[100:103], v[206:209], v[116:119]
	v_mfma_f32_16x16x32_bf16 v[108:111], v[84:87], v[214:217], v[108:111]
	v_mfma_f32_16x16x32_bf16 v[92:95], v[100:103], v[214:217], v[92:95]
	v_mfma_f32_16x16x32_bf16 v[76:79], v[84:87], v[222:225], v[76:79]
	v_mfma_f32_16x16x32_bf16 v[68:71], v[100:103], v[222:225], v[68:71]
	v_mfma_f32_16x16x32_bf16 v[138:141], v[162:165], v[194:197], v[138:141]
	v_mfma_f32_16x16x32_bf16 v[130:133], v[186:189], v[194:197], v[130:133]
	v_mfma_f32_16x16x32_bf16 v[120:123], v[162:165], v[202:205], v[120:123]
	v_mfma_f32_16x16x32_bf16 v[112:115], v[186:189], v[202:205], v[112:115]
	v_mfma_f32_16x16x32_bf16 v[104:107], v[162:165], v[210:213], v[104:107]
	v_mfma_f32_16x16x32_bf16 v[88:91], v[186:189], v[210:213], v[88:91]
	v_mfma_f32_16x16x32_bf16 v[72:75], v[162:165], v[218:221], v[72:75]
	v_mfma_f32_16x16x32_bf16 v[64:67], v[186:189], v[218:221], v[64:67]
	v_mfma_f32_16x16x32_bf16 v[138:141], v[182:185], v[198:201], v[138:141]
	v_mfma_f32_16x16x32_bf16 v[130:133], v[190:193], v[198:201], v[130:133]
	v_mfma_f32_16x16x32_bf16 v[120:123], v[182:185], v[206:209], v[120:123]
	v_mfma_f32_16x16x32_bf16 v[112:115], v[190:193], v[206:209], v[112:115]
	v_mfma_f32_16x16x32_bf16 v[104:107], v[182:185], v[214:217], v[104:107]
	v_mfma_f32_16x16x32_bf16 v[88:91], v[190:193], v[214:217], v[88:91]
	v_mfma_f32_16x16x32_bf16 v[72:75], v[182:185], v[222:225], v[72:75]
	v_mfma_f32_16x16x32_bf16 v[64:67], v[190:193], v[222:225], v[64:67]
	s_barrier
	s_add_u32 s22, s20, 0x8000
	s_addc_u32 s23, s21, 0
	s_add_i32 s63, s63, s42
	s_mov_b32 m0, s63
	ds_read_b128 v[194:197], v180 offset:49152
	ds_read_b128 v[198:201], v180 offset:50176
	ds_read_b128 v[202:205], v180 offset:51200
	ds_read_b128 v[206:209], v180 offset:52224
	ds_read_b128 v[210:213], v180 offset:53248
	ds_read_b128 v[214:217], v180 offset:54272
	ds_read_b128 v[218:221], v180 offset:55296
	ds_read_b128 v[222:225], v180 offset:56320
	global_load_lds_dwordx4 v150, s[22:23]
	s_add_i32 m0, s63, 0x2000
	s_add_u32 s20, s20, 0xc000
	s_addc_u32 s21, s21, 0
	global_load_lds_dwordx4 v146, s[22:23]
	s_add_i32 s22, s64, s42
	s_mov_b32 m0, s22
	s_nop 0
	global_load_lds_dwordx4 v150, s[20:21]
	s_add_i32 m0, s22, 0x2000
	s_nop 0
	global_load_lds_dwordx4 v146, s[20:21]
	s_mov_b32 m0, s51
	s_nop 0
	global_load_lds_dwordx4 v152, s[18:19]
	s_mov_b32 m0, s52
	s_nop 0
	global_load_lds_dwordx4 v148, s[18:19]
	s_waitcnt vmcnt(8)
	s_waitcnt lgkmcnt(0)
	s_barrier
	v_mfma_f32_16x16x32_bf16 v[60:63], v[80:83], v[194:197], v[60:63]
	v_mfma_f32_16x16x32_bf16 v[52:55], v[96:99], v[194:197], v[52:55]
	v_mfma_f32_16x16x32_bf16 v[44:47], v[80:83], v[202:205], v[44:47]
	v_mfma_f32_16x16x32_bf16 v[36:39], v[96:99], v[202:205], v[36:39]
	v_mfma_f32_16x16x32_bf16 v[28:31], v[80:83], v[210:213], v[28:31]
	v_mfma_f32_16x16x32_bf16 v[20:23], v[96:99], v[210:213], v[20:23]
	v_mfma_f32_16x16x32_bf16 v[12:15], v[80:83], v[218:221], v[12:15]
	v_mfma_f32_16x16x32_bf16 v[4:7], v[96:99], v[218:221], v[4:7]
	v_mfma_f32_16x16x32_bf16 v[60:63], v[84:87], v[198:201], v[60:63]
	v_mfma_f32_16x16x32_bf16 v[52:55], v[100:103], v[198:201], v[52:55]
	v_mfma_f32_16x16x32_bf16 v[44:47], v[84:87], v[206:209], v[44:47]
	v_mfma_f32_16x16x32_bf16 v[36:39], v[100:103], v[206:209], v[36:39]
	v_mfma_f32_16x16x32_bf16 v[28:31], v[84:87], v[214:217], v[28:31]
	v_mfma_f32_16x16x32_bf16 v[20:23], v[100:103], v[214:217], v[20:23]
	v_mfma_f32_16x16x32_bf16 v[12:15], v[84:87], v[222:225], v[12:15]
	v_mfma_f32_16x16x32_bf16 v[4:7], v[100:103], v[222:225], v[4:7]
	v_mfma_f32_16x16x32_bf16 v[56:59], v[162:165], v[194:197], v[56:59]
	v_mfma_f32_16x16x32_bf16 v[48:51], v[186:189], v[194:197], v[48:51]
	v_mfma_f32_16x16x32_bf16 v[40:43], v[162:165], v[202:205], v[40:43]
	v_mfma_f32_16x16x32_bf16 v[32:35], v[186:189], v[202:205], v[32:35]
	v_mfma_f32_16x16x32_bf16 v[24:27], v[162:165], v[210:213], v[24:27]
	v_mfma_f32_16x16x32_bf16 v[16:19], v[186:189], v[210:213], v[16:19]
	v_mfma_f32_16x16x32_bf16 v[8:11], v[162:165], v[218:221], v[8:11]
	v_mfma_f32_16x16x32_bf16 v[0:3], v[186:189], v[218:221], v[0:3]
	v_mfma_f32_16x16x32_bf16 v[56:59], v[182:185], v[198:201], v[56:59]
	v_mfma_f32_16x16x32_bf16 v[48:51], v[190:193], v[198:201], v[48:51]
	v_mfma_f32_16x16x32_bf16 v[40:43], v[182:185], v[206:209], v[40:43]
	v_mfma_f32_16x16x32_bf16 v[32:35], v[190:193], v[206:209], v[32:35]
	v_mfma_f32_16x16x32_bf16 v[24:27], v[182:185], v[214:217], v[24:27]
	v_mfma_f32_16x16x32_bf16 v[16:19], v[190:193], v[214:217], v[16:19]
	v_mfma_f32_16x16x32_bf16 v[8:11], v[182:185], v[222:225], v[8:11]
	v_mfma_f32_16x16x32_bf16 v[0:3], v[190:193], v[222:225], v[0:3]
	s_barrier
	s_add_i32 s62, s62, 2
	s_add_u32 s16, s16, 0x10000
	s_addc_u32 s17, s17, 0
	s_add_u32 s60, s60, 0x10000
	s_addc_u32 s61, s61, 0
	.p2align	6

; #define PG8_STAGE(bufoff, gbase, voff) do { _Pragma("unroll") for (int _i = 0; _i < 2; ++_i) \
;         __builtin_amdgcn_global_load_lds((const unsigned*)((const char*)(gbase) + (voff)[_i]), (PG8_LAS unsigned*)(lds + (bufoff) + ldsw + _i * 8192), 16, 0, 0); } while (0)
; #define PG8_LDA(dst, b, h) do { _Pragma("unroll") for (int m = 0; m < 4; ++m) _Pragma("unroll") for (int k = 0; k < 2; ++k) dst[m][k] = *(const PG8_LAS bf16x8*)(lds + PG8_SA(b, h) + aoff + m * 2048 + k * 1024); } while (0)
; #define PG8_LDB(dst, b, h) do { _Pragma("unroll") for (int n = 0; n < 2; ++n) _Pragma("unroll") for (int k = 0; k < 2; ++k) dst[n][k] = *(const PG8_LAS bf16x8*)(lds + PG8_SB(b, h) + boff + n * 2048 + k * 1024); } while (0)
; #define PG8_MMA(ai, bj, At, Bt) do { __builtin_amdgcn_s_setprio(1); _Pragma("unroll") for (int m = 0; m < 4; ++m) _Pragma("unroll") for (int n = 0; n < 2; ++n) _Pragma("unroll") for (int k = 0; k < 2; ++k) \
;         acc[ai][bj][m][n] = __builtin_amdgcn_mfma_f32_16x16x32_bf16(Bt[n][k], At[m][k], acc[ai][bj][m][n], 0, 0, 0); __builtin_amdgcn_s_setprio(0); } while (0)
; #define PG8_WAIT_V(n) asm volatile("s_waitcnt vmcnt(" #n ")" ::: "memory")
; #define PG8_WAIT_L(n) asm volatile("s_waitcnt lgkmcnt(" #n ")" ::: "memory")
; #define PG8_BAR __builtin_amdgcn_s_barrier()
; #define PG8_SCHED __builtin_amdgcn_sched_barrier(0)
; template <class Epi, class Sched, bool ALIGN_EPI>
; __device__ __forceinline__ void gemm_phase(PG8_LAS unsigned char* lds, const Gemm g, const Sched& S, const Epi& E, const int tid) {
;     ...
;             PG8_LDB(B0, 0, 0); PG8_LDB(B1, 0, 1); PG8_SCHED; PG8_LDA(At, 0, 0); PG8_STAGE(PG8_SA(1, 1), a1 + hstepA, voffA);
;             PG8_WAIT_V(8); PG8_WAIT_L(0); PG8_BAR; PG8_MMA(0, 0, At, B0); PG8_MMA(0, 1, At, B1); PG8_BAR; PG8_SCHED;
;             PG8_LDA(At, 0, 1); PG8_STAGE(PG8_SB(0, 0), b2, voffB); PG8_STAGE(PG8_SB(0, 1), b2 + hstepB, voffB); PG8_STAGE(PG8_SA(0, 0), a2, voffA);
;             PG8_WAIT_V(8); PG8_WAIT_L(0); PG8_BAR; PG8_MMA(1, 0, At, B0); PG8_MMA(1, 1, At, B1); PG8_BAR; PG8_SCHED;
;             PG8_LDB(B0, 1, 0); PG8_LDB(B1, 1, 1); PG8_SCHED; PG8_LDA(At, 1, 0); PG8_STAGE(PG8_SA(0, 1), a2 + hstepA, voffA);
;             PG8_WAIT_V(8); PG8_WAIT_L(0); PG8_BAR; PG8_MMA(0, 0, At, B0); PG8_MMA(0, 1, At, B1); PG8_BAR; PG8_SCHED;
.Lsprio_1:
	s_barrier
	v_mfma_f32_16x16x32_bf16 v[142:145], v[48:51], v[188:191], 0
	v_mfma_f32_16x16x32_bf16 v[138:141], v[64:67], v[188:191], 0
	v_mfma_f32_16x16x32_bf16 v[124:127], v[48:51], v[196:199], 0
	v_mfma_f32_16x16x32_bf16 v[120:123], v[64:67], v[196:199], 0
	v_mfma_f32_16x16x32_bf16 v[108:111], v[48:51], v[204:207], 0
	v_mfma_f32_16x16x32_bf16 v[104:107], v[64:67], v[204:207], 0
	v_mfma_f32_16x16x32_bf16 v[92:95], v[48:51], v[216:219], 0
	v_mfma_f32_16x16x32_bf16 v[88:91], v[64:67], v[216:219], 0
	v_mfma_f32_16x16x32_bf16 v[142:145], v[52:55], v[192:195], v[142:145]
	v_mfma_f32_16x16x32_bf16 v[138:141], v[68:71], v[192:195], v[138:141]
	v_mfma_f32_16x16x32_bf16 v[124:127], v[52:55], v[200:203], v[124:127]
	v_mfma_f32_16x16x32_bf16 v[120:123], v[68:71], v[200:203], v[120:123]
	v_mfma_f32_16x16x32_bf16 v[108:111], v[52:55], v[212:215], v[108:111]
	v_mfma_f32_16x16x32_bf16 v[104:107], v[68:71], v[212:215], v[104:107]
	v_mfma_f32_16x16x32_bf16 v[92:95], v[52:55], v[220:223], v[92:95]
	v_mfma_f32_16x16x32_bf16 v[88:91], v[68:71], v[220:223], v[88:91]
	v_mfma_f32_16x16x32_bf16 v[134:137], v[146:149], v[188:191], 0
	v_mfma_f32_16x16x32_bf16 v[130:133], v[180:183], v[188:191], 0
	v_mfma_f32_16x16x32_bf16 v[116:119], v[146:149], v[196:199], 0
	v_mfma_f32_16x16x32_bf16 v[112:115], v[180:183], v[196:199], 0
	v_mfma_f32_16x16x32_bf16 v[100:103], v[146:149], v[204:207], 0
	v_mfma_f32_16x16x32_bf16 v[96:99], v[180:183], v[204:207], 0
	v_mfma_f32_16x16x32_bf16 v[84:87], v[146:149], v[216:219], 0
	v_mfma_f32_16x16x32_bf16 v[80:83], v[180:183], v[216:219], 0
	v_mfma_f32_16x16x32_bf16 v[134:137], v[150:153], v[192:195], v[134:137]
	v_mfma_f32_16x16x32_bf16 v[130:133], v[184:187], v[192:195], v[130:133]
	v_mfma_f32_16x16x32_bf16 v[116:119], v[150:153], v[200:203], v[116:119]
	v_mfma_f32_16x16x32_bf16 v[112:115], v[184:187], v[200:203], v[112:115]
	v_mfma_f32_16x16x32_bf16 v[100:103], v[150:153], v[212:215], v[100:103]
	v_mfma_f32_16x16x32_bf16 v[96:99], v[184:187], v[212:215], v[96:99]
	v_mfma_f32_16x16x32_bf16 v[84:87], v[150:153], v[220:223], v[84:87]
	v_mfma_f32_16x16x32_bf16 v[80:83], v[184:187], v[220:223], v[80:83]
	s_barrier
	s_add_i32 s82, s82, s59
	s_mov_b32 m0, s82
	ds_read_b128 v[188:191], v210 offset:16384
	ds_read_b128 v[192:195], v210 offset:17408
	ds_read_b128 v[196:199], v210 offset:18432
	ds_read_b128 v[200:203], v210 offset:19456
	ds_read_b128 v[204:207], v210 offset:20480
	ds_read_b128 v[212:215], v210 offset:21504
	ds_read_b128 v[216:219], v210 offset:22528
	ds_read_b128 v[220:223], v210 offset:23552
	global_load_lds_dwordx4 v156, s[52:53]
	s_add_i32 m0, s82, 0x2000
	s_add_u32 s82, s52, 0x4000
	s_addc_u32 s83, s53, 0
	s_add_i32 s84, s84, s59
	global_load_lds_dwordx4 v160, s[52:53]
	s_mov_b32 m0, s84
	s_nop 0
	global_load_lds_dwordx4 v156, s[82:83]
	s_add_i32 m0, s84, 0x2000
	s_nop 0
	global_load_lds_dwordx4 v160, s[82:83]
	s_mov_b32 m0, s62
	s_nop 0
	global_load_lds_dwordx4 v154, s[54:55]
	s_mov_b32 m0, s63
	s_nop 0
	global_load_lds_dwordx4 v158, s[54:55]
	s_waitcnt vmcnt(8)
	s_waitcnt lgkmcnt(0)
	s_barrier
	v_mfma_f32_16x16x32_bf16 v[76:79], v[48:51], v[188:191], 0
	v_mfma_f32_16x16x32_bf16 v[72:75], v[64:67], v[188:191], 0
	v_mfma_f32_16x16x32_bf16 v[44:47], v[48:51], v[196:199], 0
	v_mfma_f32_16x16x32_bf16 v[40:43], v[64:67], v[196:199], 0
	v_mfma_f32_16x16x32_bf16 v[28:31], v[48:51], v[204:207], 0
	v_mfma_f32_16x16x32_bf16 v[24:27], v[64:67], v[204:207], 0
	v_mfma_f32_16x16x32_bf16 v[12:15], v[48:51], v[216:219], 0
	v_mfma_f32_16x16x32_bf16 v[8:11], v[64:67], v[216:219], 0
	v_mfma_f32_16x16x32_bf16 v[76:79], v[52:55], v[192:195], v[76:79]
	v_mfma_f32_16x16x32_bf16 v[72:75], v[68:71], v[192:195], v[72:75]
	v_mfma_f32_16x16x32_bf16 v[44:47], v[52:55], v[200:203], v[44:47]
	v_mfma_f32_16x16x32_bf16 v[40:43], v[68:71], v[200:203], v[40:43]
	v_mfma_f32_16x16x32_bf16 v[28:31], v[52:55], v[212:215], v[28:31]
	v_mfma_f32_16x16x32_bf16 v[24:27], v[68:71], v[212:215], v[24:27]
	v_mfma_f32_16x16x32_bf16 v[12:15], v[52:55], v[220:223], v[12:15]
	v_mfma_f32_16x16x32_bf16 v[8:11], v[68:71], v[220:223], v[8:11]
	v_mfma_f32_16x16x32_bf16 v[36:39], v[146:149], v[196:199], 0
	v_mfma_f32_16x16x32_bf16 v[32:35], v[180:183], v[196:199], 0
	v_mfma_f32_16x16x32_bf16 v[20:23], v[146:149], v[204:207], 0
	v_mfma_f32_16x16x32_bf16 v[16:19], v[180:183], v[204:207], 0
	v_mfma_f32_16x16x32_bf16 v[4:7], v[146:149], v[216:219], 0
	v_mfma_f32_16x16x32_bf16 v[0:3], v[180:183], v[216:219], 0
	v_mfma_f32_16x16x32_bf16 v[48:51], v[146:149], v[188:191], 0
	v_mfma_f32_16x16x32_bf16 v[52:55], v[180:183], v[188:191], 0
	v_mfma_f32_16x16x32_bf16 v[36:39], v[150:153], v[200:203], v[36:39]
	v_mfma_f32_16x16x32_bf16 v[32:35], v[184:187], v[200:203], v[32:35]
	v_mfma_f32_16x16x32_bf16 v[20:23], v[150:153], v[212:215], v[20:23]
	v_mfma_f32_16x16x32_bf16 v[16:19], v[184:187], v[212:215], v[16:19]
	v_mfma_f32_16x16x32_bf16 v[4:7], v[150:153], v[220:223], v[4:7]
	v_mfma_f32_16x16x32_bf16 v[0:3], v[184:187], v[220:223], v[0:3]
	v_mfma_f32_16x16x32_bf16 v[48:51], v[150:153], v[192:195], v[48:51]
	v_mfma_f32_16x16x32_bf16 v[52:55], v[184:187], v[192:195], v[52:55]
	s_barrier
	s_add_i32 s82, 0, 0x18000
	s_add_i32 s83, 0, 0x1c000
	ds_read_b128 v[56:59], v166 offset:32768
	ds_read_b128 v[60:63], v166 offset:33792
	ds_read_b128 v[64:67], v166 offset:34816
	ds_read_b128 v[68:71], v166 offset:35840
	ds_read_b128 v[146:149], v166 offset:49152
	ds_read_b128 v[150:153], v166 offset:50176
	ds_read_b128 v[180:183], v166 offset:51200
	ds_read_b128 v[184:187], v166 offset:52224
	s_add_u32 s54, s54, 0x4000
	s_addc_u32 s55, s55, 0
	s_mov_b32 m0, s64
	ds_read_b128 v[188:191], v210 offset:32768
	ds_read_b128 v[192:195], v210 offset:33792
	ds_read_b128 v[196:199], v210 offset:34816
	ds_read_b128 v[200:203], v210 offset:35840
	ds_read_b128 v[204:207], v210 offset:36864
	ds_read_b128 v[212:215], v210 offset:37888
	ds_read_b128 v[216:219], v210 offset:38912
	ds_read_b128 v[220:223], v210 offset:39936
	global_load_lds_dwordx4 v154, s[54:55]
	s_mov_b32 m0, s65
	s_nop 0
	global_load_lds_dwordx4 v158, s[54:55]
	s_waitcnt vmcnt(8)
	s_waitcnt lgkmcnt(0)
	s_barrier
; #define PG8_STAGE(bufoff, gbase, voff) do { _Pragma("unroll") for (int _i = 0; _i < 2; ++_i) \
;         __builtin_amdgcn_global_load_lds((const unsigned*)((const char*)(gbase) + (voff)[_i]), (PG8_LAS unsigned*)(lds + (bufoff) + ldsw + _i * 8192), 16, 0, 0); } while (0)
; #define PG8_LDA(dst, b, h) do { _Pragma("unroll") for (int m = 0; m < 4; ++m) _Pragma("unroll") for (int k = 0; k < 2; ++k) dst[m][k] = *(const PG8_LAS bf16x8*)(lds + PG8_SA(b, h) + aoff + m * 2048 + k * 1024); } while (0)
; #define PG8_LDB(dst, b, h) do { _Pragma("unroll") for (int n = 0; n < 2; ++n) _Pragma("unroll") for (int k = 0; k < 2; ++k) dst[n][k] = *(const PG8_LAS bf16x8*)(lds + PG8_SB(b, h) + boff + n * 2048 + k * 1024); } while (0)
; #define PG8_MMA(ai, bj, At, Bt) do { __builtin_amdgcn_s_setprio(1); _Pragma("unroll") for (int m = 0; m < 4; ++m) _Pragma("unroll") for (int n = 0; n < 2; ++n) _Pragma("unroll") for (int k = 0; k < 2; ++k) \
;         acc[ai][bj][m][n] = __builtin_amdgcn_mfma_f32_16x16x32_bf16(Bt[n][k], At[m][k], acc[ai][bj][m][n], 0, 0, 0); __builtin_amdgcn_s_setprio(0); } while (0)
; #define PG8_WAIT_V(n) asm volatile("s_waitcnt vmcnt(" #n ")" ::: "memory")
; #define PG8_WAIT_L(n) asm volatile("s_waitcnt lgkmcnt(" #n ")" ::: "memory")
; #define PG8_BAR __builtin_amdgcn_s_barrier()
; #define PG8_SCHED __builtin_amdgcn_sched_barrier(0)
; template <class Epi, class Sched, bool ALIGN_EPI>
; __device__ __forceinline__ void gemm_phase(PG8_LAS unsigned char* lds, const Gemm g, const Sched& S, const Epi& E, const int tid) {
;     ...
;             PG8_LDB(B0, 1, 0); PG8_LDB(B1, 1, 1); PG8_SCHED; PG8_LDA(At, 1, 0); PG8_STAGE(PG8_SA(0, 1), a2 + hstepA, voffA);
;             PG8_WAIT_V(8); PG8_WAIT_L(0); PG8_BAR; PG8_MMA(0, 0, At, B0); PG8_MMA(0, 1, At, B1); PG8_BAR; PG8_SCHED;
;             PG8_LDA(At, 1, 1); PG8_STAGE(PG8_SB(1, 0), b3, voffB); PG8_STAGE(PG8_SB(1, 1), b3 + hstepB, voffB); PG8_STAGE(PG8_SA(1, 0), a3, voffA);
;             PG8_WAIT_V(8); PG8_WAIT_L(0); PG8_BAR; PG8_MMA(1, 0, At, B0); PG8_MMA(1, 1, At, B1); PG8_BAR; PG8_SCHED;
;         }
	v_mfma_f32_16x16x32_bf16 v[142:145], v[56:59], v[188:191], v[142:145]
	v_mfma_f32_16x16x32_bf16 v[138:141], v[64:67], v[188:191], v[138:141]
	v_mfma_f32_16x16x32_bf16 v[124:127], v[56:59], v[196:199], v[124:127]
	v_mfma_f32_16x16x32_bf16 v[120:123], v[64:67], v[196:199], v[120:123]
	v_mfma_f32_16x16x32_bf16 v[108:111], v[56:59], v[204:207], v[108:111]
	v_mfma_f32_16x16x32_bf16 v[104:107], v[64:67], v[204:207], v[104:107]
	v_mfma_f32_16x16x32_bf16 v[92:95], v[56:59], v[216:219], v[92:95]
	v_mfma_f32_16x16x32_bf16 v[88:91], v[64:67], v[216:219], v[88:91]
	v_mfma_f32_16x16x32_bf16 v[142:145], v[60:63], v[192:195], v[142:145]
	v_mfma_f32_16x16x32_bf16 v[138:141], v[68:71], v[192:195], v[138:141]
	v_mfma_f32_16x16x32_bf16 v[124:127], v[60:63], v[200:203], v[124:127]
	v_mfma_f32_16x16x32_bf16 v[120:123], v[68:71], v[200:203], v[120:123]
	v_mfma_f32_16x16x32_bf16 v[108:111], v[60:63], v[212:215], v[108:111]
	v_mfma_f32_16x16x32_bf16 v[104:107], v[68:71], v[212:215], v[104:107]
	v_mfma_f32_16x16x32_bf16 v[92:95], v[60:63], v[220:223], v[92:95]
	v_mfma_f32_16x16x32_bf16 v[88:91], v[68:71], v[220:223], v[88:91]
	v_mfma_f32_16x16x32_bf16 v[134:137], v[146:149], v[188:191], v[134:137]
	v_mfma_f32_16x16x32_bf16 v[130:133], v[180:183], v[188:191], v[130:133]
	v_mfma_f32_16x16x32_bf16 v[116:119], v[146:149], v[196:199], v[116:119]
	v_mfma_f32_16x16x32_bf16 v[112:115], v[180:183], v[196:199], v[112:115]
	v_mfma_f32_16x16x32_bf16 v[100:103], v[146:149], v[204:207], v[100:103]
	v_mfma_f32_16x16x32_bf16 v[96:99], v[180:183], v[204:207], v[96:99]
	v_mfma_f32_16x16x32_bf16 v[84:87], v[146:149], v[216:219], v[84:87]
	v_mfma_f32_16x16x32_bf16 v[80:83], v[180:183], v[216:219], v[80:83]
	v_mfma_f32_16x16x32_bf16 v[134:137], v[150:153], v[192:195], v[134:137]
	v_mfma_f32_16x16x32_bf16 v[130:133], v[184:187], v[192:195], v[130:133]
	v_mfma_f32_16x16x32_bf16 v[116:119], v[150:153], v[200:203], v[116:119]
	v_mfma_f32_16x16x32_bf16 v[112:115], v[184:187], v[200:203], v[112:115]
	v_mfma_f32_16x16x32_bf16 v[100:103], v[150:153], v[212:215], v[100:103]
	v_mfma_f32_16x16x32_bf16 v[96:99], v[184:187], v[212:215], v[96:99]
	v_mfma_f32_16x16x32_bf16 v[84:87], v[150:153], v[220:223], v[84:87]
	v_mfma_f32_16x16x32_bf16 v[80:83], v[184:187], v[220:223], v[80:83]
	s_barrier
	s_add_u32 s54, s52, 0x8000
	s_addc_u32 s55, s53, 0
	s_add_i32 s82, s82, s59
	s_mov_b32 m0, s82
	ds_read_b128 v[188:191], v210 offset:49152
	ds_read_b128 v[192:195], v210 offset:50176
	ds_read_b128 v[196:199], v210 offset:51200
	ds_read_b128 v[200:203], v210 offset:52224
	ds_read_b128 v[204:207], v210 offset:53248
	ds_read_b128 v[212:215], v210 offset:54272
	ds_read_b128 v[216:219], v210 offset:55296
	ds_read_b128 v[220:223], v210 offset:56320
	global_load_lds_dwordx4 v156, s[54:55]
	s_add_i32 m0, s82, 0x2000
	s_add_u32 s52, s52, 0xc000
	s_addc_u32 s53, s53, 0
	global_load_lds_dwordx4 v160, s[54:55]
	s_add_i32 s54, s83, s59
	s_mov_b32 m0, s54
	s_nop 0
	global_load_lds_dwordx4 v156, s[52:53]
	s_add_i32 m0, s54, 0x2000
	s_nop 0
	global_load_lds_dwordx4 v160, s[52:53]
	s_mov_b32 m0, s66
	s_nop 0
	global_load_lds_dwordx4 v154, s[12:13]
	s_mov_b32 m0, s67
	s_nop 0
	global_load_lds_dwordx4 v158, s[12:13]
	s_waitcnt vmcnt(8)
	s_waitcnt lgkmcnt(0)
	s_barrier
	v_mfma_f32_16x16x32_bf16 v[76:79], v[56:59], v[188:191], v[76:79]
	v_mfma_f32_16x16x32_bf16 v[72:75], v[64:67], v[188:191], v[72:75]
	v_mfma_f32_16x16x32_bf16 v[44:47], v[56:59], v[196:199], v[44:47]
	v_mfma_f32_16x16x32_bf16 v[40:43], v[64:67], v[196:199], v[40:43]
	v_mfma_f32_16x16x32_bf16 v[28:31], v[56:59], v[204:207], v[28:31]
	v_mfma_f32_16x16x32_bf16 v[24:27], v[64:67], v[204:207], v[24:27]
	v_mfma_f32_16x16x32_bf16 v[12:15], v[56:59], v[216:219], v[12:15]
	v_mfma_f32_16x16x32_bf16 v[8:11], v[64:67], v[216:219], v[8:11]
	v_mfma_f32_16x16x32_bf16 v[76:79], v[60:63], v[192:195], v[76:79]
	v_mfma_f32_16x16x32_bf16 v[72:75], v[68:71], v[192:195], v[72:75]
	v_mfma_f32_16x16x32_bf16 v[44:47], v[60:63], v[200:203], v[44:47]
	v_mfma_f32_16x16x32_bf16 v[40:43], v[68:71], v[200:203], v[40:43]
	v_mfma_f32_16x16x32_bf16 v[28:31], v[60:63], v[212:215], v[28:31]
	v_mfma_f32_16x16x32_bf16 v[24:27], v[68:71], v[212:215], v[24:27]
	v_mfma_f32_16x16x32_bf16 v[12:15], v[60:63], v[220:223], v[12:15]
	v_mfma_f32_16x16x32_bf16 v[8:11], v[68:71], v[220:223], v[8:11]
	v_mfma_f32_16x16x32_bf16 v[48:51], v[146:149], v[188:191], v[48:51]
	v_mfma_f32_16x16x32_bf16 v[60:63], v[150:153], v[192:195], v[48:51]
	v_mfma_f32_16x16x32_bf16 v[48:51], v[180:183], v[188:191], v[52:55]
	v_mfma_f32_16x16x32_bf16 v[36:39], v[146:149], v[196:199], v[36:39]
	v_mfma_f32_16x16x32_bf16 v[32:35], v[180:183], v[196:199], v[32:35]
	v_mfma_f32_16x16x32_bf16 v[20:23], v[146:149], v[204:207], v[20:23]
	v_mfma_f32_16x16x32_bf16 v[16:19], v[180:183], v[204:207], v[16:19]
	v_mfma_f32_16x16x32_bf16 v[4:7], v[146:149], v[216:219], v[4:7]
	v_mfma_f32_16x16x32_bf16 v[0:3], v[180:183], v[216:219], v[0:3]
	v_mfma_f32_16x16x32_bf16 v[56:59], v[184:187], v[192:195], v[48:51]
	v_mfma_f32_16x16x32_bf16 v[36:39], v[150:153], v[200:203], v[36:39]
	v_mfma_f32_16x16x32_bf16 v[32:35], v[184:187], v[200:203], v[32:35]
	v_mfma_f32_16x16x32_bf16 v[20:23], v[150:153], v[212:215], v[20:23]
	v_mfma_f32_16x16x32_bf16 v[16:19], v[184:187], v[212:215], v[16:19]
	v_mfma_f32_16x16x32_bf16 v[4:7], v[150:153], v[220:223], v[4:7]
	v_mfma_f32_16x16x32_bf16 v[0:3], v[184:187], v[220:223], v[0:3]
	s_barrier
	s_add_i32 s81, s81, 2
	s_add_u32 s10, s10, 0x10000
	s_addc_u32 s11, s11, 0
	s_add_u32 s79, s79, 0x10000
	s_addc_u32 s80, s80, 0
	.p2align	6

; #define PG8_STAGE(bufoff, gbase, voff) do { _Pragma("unroll") for (int _i = 0; _i < 2; ++_i) \
;         __builtin_amdgcn_global_load_lds((const unsigned*)((const char*)(gbase) + (voff)[_i]), (PG8_LAS unsigned*)(lds + (bufoff) + ldsw + _i * 8192), 16, 0, 0); } while (0)
; #define PG8_LDA(dst, b, h) do { _Pragma("unroll") for (int m = 0; m < 4; ++m) _Pragma("unroll") for (int k = 0; k < 2; ++k) dst[m][k] = *(const PG8_LAS bf16x8*)(lds + PG8_SA(b, h) + aoff + m * 2048 + k * 1024); } while (0)
; #define PG8_LDB(dst, b, h) do { _Pragma("unroll") for (int n = 0; n < 2; ++n) _Pragma("unroll") for (int k = 0; k < 2; ++k) dst[n][k] = *(const PG8_LAS bf16x8*)(lds + PG8_SB(b, h) + boff + n * 2048 + k * 1024); } while (0)
; #define PG8_MMA(ai, bj, At, Bt) do { __builtin_amdgcn_s_setprio(1); _Pragma("unroll") for (int m = 0; m < 4; ++m) _Pragma("unroll") for (int n = 0; n < 2; ++n) _Pragma("unroll") for (int k = 0; k < 2; ++k) \
;         acc[ai][bj][m][n] = __builtin_amdgcn_mfma_f32_16x16x32_bf16(Bt[n][k], At[m][k], acc[ai][bj][m][n], 0, 0, 0); __builtin_amdgcn_s_setprio(0); } while (0)
; #define PG8_WAIT_V(n) asm volatile("s_waitcnt vmcnt(" #n ")" ::: "memory")
; #define PG8_WAIT_L(n) asm volatile("s_waitcnt lgkmcnt(" #n ")" ::: "memory")
; #define PG8_BAR __builtin_amdgcn_s_barrier()
; #define PG8_SCHED __builtin_amdgcn_sched_barrier(0)
; template <class Epi, class Sched, bool ALIGN_EPI>
; __device__ __forceinline__ void gemm_phase(PG8_LAS unsigned char* lds, const Gemm g, const Sched& S, const Epi& E, const int tid) {
;     ...
;             PG8_LDB(B0, 0, 0); PG8_LDB(B1, 0, 1); PG8_SCHED; PG8_LDA(At, 0, 0); PG8_STAGE(PG8_SA(1, 1), a1 + hstepA, voffA);
;             PG8_WAIT_V(8); PG8_WAIT_L(0); PG8_BAR; PG8_MMA(0, 0, At, B0); PG8_MMA(0, 1, At, B1); PG8_BAR; PG8_SCHED;
;             PG8_LDA(At, 0, 1); PG8_STAGE(PG8_SB(0, 0), b2, voffB); PG8_STAGE(PG8_SB(0, 1), b2 + hstepB, voffB); PG8_STAGE(PG8_SA(0, 0), a2, voffA);
;             PG8_WAIT_V(8); PG8_WAIT_L(0); PG8_BAR; PG8_MMA(1, 0, At, B0); PG8_MMA(1, 1, At, B1); PG8_BAR; PG8_SCHED;
;             PG8_LDB(B0, 1, 0); PG8_LDB(B1, 1, 1); PG8_SCHED; PG8_LDA(At, 1, 0); PG8_STAGE(PG8_SA(0, 1), a2 + hstepA, voffA);
.Lsprio_2:
	s_barrier
	v_mfma_f32_16x16x32_bf16 v[142:145], v[88:91], v[162:165], 0
	v_mfma_f32_16x16x32_bf16 v[138:141], v[100:103], v[162:165], 0
	v_mfma_f32_16x16x32_bf16 v[124:127], v[88:91], v[172:175], 0
	v_mfma_f32_16x16x32_bf16 v[120:123], v[100:103], v[172:175], 0
	v_mfma_f32_16x16x32_bf16 v[104:107], v[88:91], v[196:199], 0
	v_mfma_f32_16x16x32_bf16 v[96:99], v[100:103], v[196:199], 0
	v_mfma_f32_16x16x32_bf16 v[76:79], v[88:91], v[204:207], 0
	v_mfma_f32_16x16x32_bf16 v[72:75], v[100:103], v[204:207], 0
	v_mfma_f32_16x16x32_bf16 v[142:145], v[92:95], v[166:169], v[142:145]
	v_mfma_f32_16x16x32_bf16 v[138:141], v[108:111], v[166:169], v[138:141]
	v_mfma_f32_16x16x32_bf16 v[124:127], v[92:95], v[188:191], v[124:127]
	v_mfma_f32_16x16x32_bf16 v[120:123], v[108:111], v[188:191], v[120:123]
	v_mfma_f32_16x16x32_bf16 v[104:107], v[92:95], v[200:203], v[104:107]
	v_mfma_f32_16x16x32_bf16 v[96:99], v[108:111], v[200:203], v[96:99]
	v_mfma_f32_16x16x32_bf16 v[76:79], v[92:95], v[208:211], v[76:79]
	v_mfma_f32_16x16x32_bf16 v[72:75], v[108:111], v[208:211], v[72:75]
	v_mfma_f32_16x16x32_bf16 v[134:137], v[146:149], v[162:165], 0
	v_mfma_f32_16x16x32_bf16 v[130:133], v[154:157], v[162:165], 0
	v_mfma_f32_16x16x32_bf16 v[116:119], v[146:149], v[172:175], 0
	v_mfma_f32_16x16x32_bf16 v[112:115], v[154:157], v[172:175], 0
	v_mfma_f32_16x16x32_bf16 v[84:87], v[146:149], v[196:199], 0
	v_mfma_f32_16x16x32_bf16 v[80:83], v[154:157], v[196:199], 0
	v_mfma_f32_16x16x32_bf16 v[68:71], v[146:149], v[204:207], 0
	v_mfma_f32_16x16x32_bf16 v[64:67], v[154:157], v[204:207], 0
	v_mfma_f32_16x16x32_bf16 v[134:137], v[150:153], v[166:169], v[134:137]
	v_mfma_f32_16x16x32_bf16 v[130:133], v[158:161], v[166:169], v[130:133]
	v_mfma_f32_16x16x32_bf16 v[116:119], v[150:153], v[188:191], v[116:119]
	v_mfma_f32_16x16x32_bf16 v[112:115], v[158:161], v[188:191], v[112:115]
	v_mfma_f32_16x16x32_bf16 v[84:87], v[150:153], v[200:203], v[84:87]
	v_mfma_f32_16x16x32_bf16 v[80:83], v[158:161], v[200:203], v[80:83]
	v_mfma_f32_16x16x32_bf16 v[68:71], v[150:153], v[208:211], v[68:71]
	v_mfma_f32_16x16x32_bf16 v[64:67], v[158:161], v[208:211], v[64:67]
	s_barrier
	s_add_i32 s54, s56, s30
	s_mov_b32 m0, s54
	ds_read_b128 v[162:165], v185 offset:16384
	ds_read_b128 v[166:169], v185 offset:17408
	ds_read_b128 v[172:175], v185 offset:18432
	ds_read_b128 v[188:191], v185 offset:19456
	ds_read_b128 v[196:199], v185 offset:20480
	ds_read_b128 v[200:203], v185 offset:21504
	ds_read_b128 v[204:207], v185 offset:22528
	ds_read_b128 v[208:211], v185 offset:23552
	global_load_lds_dwordx4 v178, s[24:25]
	s_add_i32 m0, s54, 0x2000
	s_add_u32 s54, s24, 0x4000
	s_addc_u32 s55, s25, 0
	s_add_i32 s56, s57, s30
	global_load_lds_dwordx4 v182, s[24:25]
	s_mov_b32 m0, s56
	s_nop 0
	global_load_lds_dwordx4 v178, s[54:55]
	s_add_i32 m0, s56, 0x2000
	s_nop 0
	global_load_lds_dwordx4 v182, s[54:55]
	s_mov_b32 m0, s31
	s_nop 0
	global_load_lds_dwordx4 v176, s[26:27]
	s_mov_b32 m0, s33
	s_nop 0
	global_load_lds_dwordx4 v180, s[26:27]
	s_waitcnt vmcnt(8)
	s_waitcnt lgkmcnt(0)
	s_barrier
	v_mfma_f32_16x16x32_bf16 v[60:63], v[88:91], v[162:165], 0
	v_mfma_f32_16x16x32_bf16 v[56:59], v[100:103], v[162:165], 0
	v_mfma_f32_16x16x32_bf16 v[44:47], v[88:91], v[172:175], 0
	v_mfma_f32_16x16x32_bf16 v[40:43], v[100:103], v[172:175], 0
	v_mfma_f32_16x16x32_bf16 v[28:31], v[88:91], v[196:199], 0
	v_mfma_f32_16x16x32_bf16 v[24:27], v[100:103], v[196:199], 0
	v_mfma_f32_16x16x32_bf16 v[12:15], v[88:91], v[204:207], 0
	v_mfma_f32_16x16x32_bf16 v[8:11], v[100:103], v[204:207], 0
	v_mfma_f32_16x16x32_bf16 v[60:63], v[92:95], v[166:169], v[60:63]
	v_mfma_f32_16x16x32_bf16 v[56:59], v[108:111], v[166:169], v[56:59]
	v_mfma_f32_16x16x32_bf16 v[44:47], v[92:95], v[188:191], v[44:47]
	v_mfma_f32_16x16x32_bf16 v[40:43], v[108:111], v[188:191], v[40:43]
	v_mfma_f32_16x16x32_bf16 v[28:31], v[92:95], v[200:203], v[28:31]
	v_mfma_f32_16x16x32_bf16 v[24:27], v[108:111], v[200:203], v[24:27]
	v_mfma_f32_16x16x32_bf16 v[12:15], v[92:95], v[208:211], v[12:15]
	v_mfma_f32_16x16x32_bf16 v[8:11], v[108:111], v[208:211], v[8:11]
	v_mfma_f32_16x16x32_bf16 v[52:55], v[146:149], v[162:165], 0
	v_mfma_f32_16x16x32_bf16 v[48:51], v[154:157], v[162:165], 0
	v_mfma_f32_16x16x32_bf16 v[36:39], v[146:149], v[172:175], 0
	v_mfma_f32_16x16x32_bf16 v[32:35], v[154:157], v[172:175], 0
	v_mfma_f32_16x16x32_bf16 v[20:23], v[146:149], v[196:199], 0
	v_mfma_f32_16x16x32_bf16 v[16:19], v[154:157], v[196:199], 0
	v_mfma_f32_16x16x32_bf16 v[4:7], v[146:149], v[204:207], 0
	v_mfma_f32_16x16x32_bf16 v[0:3], v[154:157], v[204:207], 0
	v_mfma_f32_16x16x32_bf16 v[52:55], v[150:153], v[166:169], v[52:55]
	v_mfma_f32_16x16x32_bf16 v[48:51], v[158:161], v[166:169], v[48:51]
	v_mfma_f32_16x16x32_bf16 v[36:39], v[150:153], v[188:191], v[36:39]
	v_mfma_f32_16x16x32_bf16 v[32:35], v[158:161], v[188:191], v[32:35]
	v_mfma_f32_16x16x32_bf16 v[20:23], v[150:153], v[200:203], v[20:23]
	v_mfma_f32_16x16x32_bf16 v[16:19], v[158:161], v[200:203], v[16:19]
	v_mfma_f32_16x16x32_bf16 v[4:7], v[150:153], v[208:211], v[4:7]
	v_mfma_f32_16x16x32_bf16 v[0:3], v[158:161], v[208:211], v[0:3]
	s_barrier
; #define PG8_STAGE(bufoff, gbase, voff) do { _Pragma("unroll") for (int _i = 0; _i < 2; ++_i) \
;         __builtin_amdgcn_global_load_lds((const unsigned*)((const char*)(gbase) + (voff)[_i]), (PG8_LAS unsigned*)(lds + (bufoff) + ldsw + _i * 8192), 16, 0, 0); } while (0)
; #define PG8_LDA(dst, b, h) do { _Pragma("unroll") for (int m = 0; m < 4; ++m) _Pragma("unroll") for (int k = 0; k < 2; ++k) dst[m][k] = *(const PG8_LAS bf16x8*)(lds + PG8_SA(b, h) + aoff + m * 2048 + k * 1024); } while (0)
; #define PG8_LDB(dst, b, h) do { _Pragma("unroll") for (int n = 0; n < 2; ++n) _Pragma("unroll") for (int k = 0; k < 2; ++k) dst[n][k] = *(const PG8_LAS bf16x8*)(lds + PG8_SB(b, h) + boff + n * 2048 + k * 1024); } while (0)
; #define PG8_MMA(ai, bj, At, Bt) do { __builtin_amdgcn_s_setprio(1); _Pragma("unroll") for (int m = 0; m < 4; ++m) _Pragma("unroll") for (int n = 0; n < 2; ++n) _Pragma("unroll") for (int k = 0; k < 2; ++k) \
;         acc[ai][bj][m][n] = __builtin_amdgcn_mfma_f32_16x16x32_bf16(Bt[n][k], At[m][k], acc[ai][bj][m][n], 0, 0, 0); __builtin_amdgcn_s_setprio(0); } while (0)
; #define PG8_WAIT_V(n) asm volatile("s_waitcnt vmcnt(" #n ")" ::: "memory")
; #define PG8_WAIT_L(n) asm volatile("s_waitcnt lgkmcnt(" #n ")" ::: "memory")
; #define PG8_BAR __builtin_amdgcn_s_barrier()
; #define PG8_SCHED __builtin_amdgcn_sched_barrier(0)
; template <class Epi, class Sched, bool ALIGN_EPI>
; __device__ __forceinline__ void gemm_phase(PG8_LAS unsigned char* lds, const Gemm g, const Sched& S, const Epi& E, const int tid) {
;     ...
;             PG8_LDB(B0, 1, 0); PG8_LDB(B1, 1, 1); PG8_SCHED; PG8_LDA(At, 1, 0); PG8_STAGE(PG8_SA(0, 1), a2 + hstepA, voffA);
;             PG8_WAIT_V(8); PG8_WAIT_L(0); PG8_BAR; PG8_MMA(0, 0, At, B0); PG8_MMA(0, 1, At, B1); PG8_BAR; PG8_SCHED;
;             PG8_LDA(At, 1, 1); PG8_STAGE(PG8_SB(1, 0), b3, voffB); PG8_STAGE(PG8_SB(1, 1), b3 + hstepB, voffB); PG8_STAGE(PG8_SA(1, 0), a3, voffA);
;             PG8_WAIT_V(8); PG8_WAIT_L(0); PG8_BAR; PG8_MMA(1, 0, At, B0); PG8_MMA(1, 1, At, B1); PG8_BAR; PG8_SCHED;
;         }
	s_add_i32 s54, 0, 0x18000
	s_add_i32 s55, 0, 0x1c000
	ds_read_b128 v[88:91], v192 offset:32768
	ds_read_b128 v[92:95], v192 offset:33792
	ds_read_b128 v[100:103], v192 offset:34816
	ds_read_b128 v[108:111], v192 offset:35840
	ds_read_b128 v[146:149], v192 offset:49152
	ds_read_b128 v[150:153], v192 offset:50176
	ds_read_b128 v[154:157], v192 offset:51200
	ds_read_b128 v[158:161], v192 offset:52224
	s_add_u32 s26, s26, s68
	s_addc_u32 s27, s27, s69
	s_mov_b32 m0, s34
	ds_read_b128 v[162:165], v185 offset:32768
	ds_read_b128 v[166:169], v185 offset:33792
	ds_read_b128 v[172:175], v185 offset:34816
	ds_read_b128 v[188:191], v185 offset:35840
	ds_read_b128 v[196:199], v185 offset:36864
	ds_read_b128 v[200:203], v185 offset:37888
	ds_read_b128 v[204:207], v185 offset:38912
	ds_read_b128 v[208:211], v185 offset:39936
	global_load_lds_dwordx4 v176, s[26:27]
	s_mov_b32 m0, s35
	s_nop 0
	global_load_lds_dwordx4 v180, s[26:27]
	s_waitcnt vmcnt(8)
	s_waitcnt lgkmcnt(0)
	s_barrier
	v_mfma_f32_16x16x32_bf16 v[142:145], v[88:91], v[162:165], v[142:145]
	v_mfma_f32_16x16x32_bf16 v[138:141], v[100:103], v[162:165], v[138:141]
	v_mfma_f32_16x16x32_bf16 v[124:127], v[88:91], v[172:175], v[124:127]
	v_mfma_f32_16x16x32_bf16 v[120:123], v[100:103], v[172:175], v[120:123]
	v_mfma_f32_16x16x32_bf16 v[104:107], v[88:91], v[196:199], v[104:107]
	v_mfma_f32_16x16x32_bf16 v[96:99], v[100:103], v[196:199], v[96:99]
	v_mfma_f32_16x16x32_bf16 v[76:79], v[88:91], v[204:207], v[76:79]
	v_mfma_f32_16x16x32_bf16 v[72:75], v[100:103], v[204:207], v[72:75]
	v_mfma_f32_16x16x32_bf16 v[142:145], v[92:95], v[166:169], v[142:145]
	v_mfma_f32_16x16x32_bf16 v[138:141], v[108:111], v[166:169], v[138:141]
	v_mfma_f32_16x16x32_bf16 v[124:127], v[92:95], v[188:191], v[124:127]
	v_mfma_f32_16x16x32_bf16 v[120:123], v[108:111], v[188:191], v[120:123]
	v_mfma_f32_16x16x32_bf16 v[104:107], v[92:95], v[200:203], v[104:107]
	v_mfma_f32_16x16x32_bf16 v[96:99], v[108:111], v[200:203], v[96:99]
	v_mfma_f32_16x16x32_bf16 v[76:79], v[92:95], v[208:211], v[76:79]
	v_mfma_f32_16x16x32_bf16 v[72:75], v[108:111], v[208:211], v[72:75]
	v_mfma_f32_16x16x32_bf16 v[134:137], v[146:149], v[162:165], v[134:137]
	v_mfma_f32_16x16x32_bf16 v[130:133], v[154:157], v[162:165], v[130:133]
	v_mfma_f32_16x16x32_bf16 v[116:119], v[146:149], v[172:175], v[116:119]
	v_mfma_f32_16x16x32_bf16 v[112:115], v[154:157], v[172:175], v[112:115]
	v_mfma_f32_16x16x32_bf16 v[84:87], v[146:149], v[196:199], v[84:87]
	v_mfma_f32_16x16x32_bf16 v[80:83], v[154:157], v[196:199], v[80:83]
	v_mfma_f32_16x16x32_bf16 v[68:71], v[146:149], v[204:207], v[68:71]
	v_mfma_f32_16x16x32_bf16 v[64:67], v[154:157], v[204:207], v[64:67]
	v_mfma_f32_16x16x32_bf16 v[134:137], v[150:153], v[166:169], v[134:137]
	v_mfma_f32_16x16x32_bf16 v[130:133], v[158:161], v[166:169], v[130:133]
	v_mfma_f32_16x16x32_bf16 v[116:119], v[150:153], v[188:191], v[116:119]
	v_mfma_f32_16x16x32_bf16 v[112:115], v[158:161], v[188:191], v[112:115]
	v_mfma_f32_16x16x32_bf16 v[84:87], v[150:153], v[200:203], v[84:87]
	v_mfma_f32_16x16x32_bf16 v[80:83], v[158:161], v[200:203], v[80:83]
	v_mfma_f32_16x16x32_bf16 v[68:71], v[150:153], v[208:211], v[68:71]
	v_mfma_f32_16x16x32_bf16 v[64:67], v[158:161], v[208:211], v[64:67]
	s_barrier
	s_add_u32 s26, s24, 0x8000
	s_addc_u32 s27, s25, 0
	s_add_i32 s54, s54, s30
	s_mov_b32 m0, s54
	ds_read_b128 v[162:165], v185 offset:49152
	ds_read_b128 v[166:169], v185 offset:50176
	ds_read_b128 v[172:175], v185 offset:51200
	ds_read_b128 v[188:191], v185 offset:52224
	ds_read_b128 v[196:199], v185 offset:53248
	ds_read_b128 v[200:203], v185 offset:54272
	ds_read_b128 v[204:207], v185 offset:55296
	ds_read_b128 v[208:211], v185 offset:56320
	global_load_lds_dwordx4 v178, s[26:27]
	s_add_i32 m0, s54, 0x2000
	s_add_u32 s24, s24, 0xc000
	s_addc_u32 s25, s25, 0
	global_load_lds_dwordx4 v182, s[26:27]
	s_add_i32 s26, s55, s30
	s_mov_b32 m0, s26
	s_nop 0
	global_load_lds_dwordx4 v178, s[24:25]
	s_add_i32 m0, s26, 0x2000
	s_nop 0
	global_load_lds_dwordx4 v182, s[24:25]
	s_mov_b32 m0, s40
	s_nop 0
	global_load_lds_dwordx4 v176, s[20:21]
	s_mov_b32 m0, s41
	s_nop 0
	global_load_lds_dwordx4 v180, s[20:21]
	s_waitcnt vmcnt(8)
	s_waitcnt lgkmcnt(0)
	s_barrier
	v_mfma_f32_16x16x32_bf16 v[60:63], v[88:91], v[162:165], v[60:63]
	v_mfma_f32_16x16x32_bf16 v[56:59], v[100:103], v[162:165], v[56:59]
	v_mfma_f32_16x16x32_bf16 v[44:47], v[88:91], v[172:175], v[44:47]
	v_mfma_f32_16x16x32_bf16 v[40:43], v[100:103], v[172:175], v[40:43]
	v_mfma_f32_16x16x32_bf16 v[28:31], v[88:91], v[196:199], v[28:31]
	v_mfma_f32_16x16x32_bf16 v[24:27], v[100:103], v[196:199], v[24:27]
	v_mfma_f32_16x16x32_bf16 v[12:15], v[88:91], v[204:207], v[12:15]
	v_mfma_f32_16x16x32_bf16 v[8:11], v[100:103], v[204:207], v[8:11]
	v_mfma_f32_16x16x32_bf16 v[60:63], v[92:95], v[166:169], v[60:63]
	v_mfma_f32_16x16x32_bf16 v[56:59], v[108:111], v[166:169], v[56:59]
	v_mfma_f32_16x16x32_bf16 v[44:47], v[92:95], v[188:191], v[44:47]
	v_mfma_f32_16x16x32_bf16 v[40:43], v[108:111], v[188:191], v[40:43]
	v_mfma_f32_16x16x32_bf16 v[28:31], v[92:95], v[200:203], v[28:31]
	v_mfma_f32_16x16x32_bf16 v[24:27], v[108:111], v[200:203], v[24:27]
	v_mfma_f32_16x16x32_bf16 v[12:15], v[92:95], v[208:211], v[12:15]
	v_mfma_f32_16x16x32_bf16 v[8:11], v[108:111], v[208:211], v[8:11]
	v_mfma_f32_16x16x32_bf16 v[52:55], v[146:149], v[162:165], v[52:55]
	v_mfma_f32_16x16x32_bf16 v[48:51], v[154:157], v[162:165], v[48:51]
	v_mfma_f32_16x16x32_bf16 v[36:39], v[146:149], v[172:175], v[36:39]
	v_mfma_f32_16x16x32_bf16 v[32:35], v[154:157], v[172:175], v[32:35]
	v_mfma_f32_16x16x32_bf16 v[20:23], v[146:149], v[196:199], v[20:23]
	v_mfma_f32_16x16x32_bf16 v[16:19], v[154:157], v[196:199], v[16:19]
	v_mfma_f32_16x16x32_bf16 v[4:7], v[146:149], v[204:207], v[4:7]
	v_mfma_f32_16x16x32_bf16 v[0:3], v[154:157], v[204:207], v[0:3]
	v_mfma_f32_16x16x32_bf16 v[52:55], v[150:153], v[166:169], v[52:55]
	v_mfma_f32_16x16x32_bf16 v[48:51], v[158:161], v[166:169], v[48:51]
	v_mfma_f32_16x16x32_bf16 v[36:39], v[150:153], v[188:191], v[36:39]
	v_mfma_f32_16x16x32_bf16 v[32:35], v[158:161], v[188:191], v[32:35]
	v_mfma_f32_16x16x32_bf16 v[20:23], v[150:153], v[200:203], v[20:23]
	v_mfma_f32_16x16x32_bf16 v[16:19], v[158:161], v[200:203], v[16:19]
	v_mfma_f32_16x16x32_bf16 v[4:7], v[150:153], v[208:211], v[4:7]
	v_mfma_f32_16x16x32_bf16 v[0:3], v[158:161], v[208:211], v[0:3]
	s_barrier
	s_add_u32 s52, s52, 0x10000
	s_addc_u32 s53, s53, 0
	s_mov_b64 s[20:21], s[22:23]
	.p2align	6
